# peerdown: drop the vmcnt ladder that over-waited on the just-issued next-token gathers (wait only where data is consumed)
# baseline (speedup 1.0000x reference)
.LBB0_1745:
	s_cmp_eq_u64 s[20:21], 0
	s_cbranch_scc0 .Lpd_steady
	s_waitcnt vmcnt(0)
.Lpd_steady:
	s_waitcnt vmcnt(20)
	v_cvt_pk_f32_fp8_e32 v[200:201], v24
	v_cvt_pk_f32_fp8_sdwa v[202:203], v24 src0_sel:WORD_1
	v_cvt_pk_f32_fp8_e32 v[204:205], v25
	v_lshlrev_b32_e32 v186, 16, v20
	v_and_b32_e32 v187, 0xffff0000, v20
	v_cvt_pk_f32_fp8_sdwa v[210:211], v25 src0_sel:WORD_1
	v_lshlrev_b32_e32 v190, 16, v21
	v_and_b32_e32 v191, 0xffff0000, v21
	v_cvt_pk_f32_fp8_e32 v[212:213], v26
	v_pk_mul_f32 v[200:201], v[200:201], v[186:187]
	v_lshlrev_b32_e32 v194, 16, v22
	v_and_b32_e32 v195, 0xffff0000, v22
	v_cvt_pk_f32_fp8_sdwa v[214:215], v26 src0_sel:WORD_1
	v_pk_fma_f32 v[200:201], v[202:203], v[190:191], v[200:201]
	v_cvt_pk_f32_fp8_e32 v[202:203], v28
	v_lshlrev_b32_e32 v198, 16, v23
	v_and_b32_e32 v199, 0xffff0000, v23
	v_cvt_pk_f32_fp8_e32 v[216:217], v27
	v_pk_fma_f32 v[200:201], v[204:205], v[194:195], v[200:201]
	v_cvt_pk_f32_fp8_sdwa v[204:205], v28 src0_sel:WORD_1
	v_lshlrev_b32_e32 v184, 16, v16
	v_and_b32_e32 v185, 0xffff0000, v16
	v_cvt_pk_f32_fp8_sdwa v[218:219], v27 src0_sel:WORD_1
	v_pk_fma_f32 v[200:201], v[210:211], v[198:199], v[200:201]
	v_cvt_pk_f32_fp8_e32 v[210:211], v29
	v_lshlrev_b32_e32 v188, 16, v17
	v_and_b32_e32 v189, 0xffff0000, v17
	v_pk_fma_f32 v[200:201], v[212:213], v[184:185], v[200:201]
	v_cvt_pk_f32_fp8_sdwa v[212:213], v29 src0_sel:WORD_1
	v_lshlrev_b32_e32 v192, 16, v18
	v_and_b32_e32 v193, 0xffff0000, v18
	v_pk_fma_f32 v[200:201], v[214:215], v[188:189], v[200:201]
	v_cvt_pk_f32_fp8_e32 v[214:215], v30
	v_pk_mul_f32 v[202:203], v[202:203], v[186:187]
	v_lshlrev_b32_e32 v196, 16, v19
	v_and_b32_e32 v197, 0xffff0000, v19
	v_pk_fma_f32 v[200:201], v[216:217], v[192:193], v[200:201]
	v_cvt_pk_f32_fp8_sdwa v[216:217], v30 src0_sel:WORD_1
	v_pk_fma_f32 v[202:203], v[204:205], v[190:191], v[202:203]
	v_cvt_pk_f32_fp8_e32 v[204:205], v32
	v_pk_fma_f32 v[200:201], v[218:219], v[196:197], v[200:201]
	v_cvt_pk_f32_fp8_e32 v[218:219], v31
	v_pk_fma_f32 v[202:203], v[210:211], v[194:195], v[202:203]
	v_cvt_pk_f32_fp8_sdwa v[210:211], v32 src0_sel:WORD_1
	v_cvt_pk_f32_fp8_sdwa v[220:221], v31 src0_sel:WORD_1
	v_pk_fma_f32 v[202:203], v[212:213], v[198:199], v[202:203]
	v_cvt_pk_f32_fp8_e32 v[212:213], v33
	v_pk_fma_f32 v[202:203], v[214:215], v[184:185], v[202:203]
	v_cvt_pk_f32_fp8_sdwa v[214:215], v33 src0_sel:WORD_1
	v_pk_fma_f32 v[202:203], v[216:217], v[188:189], v[202:203]
	v_cvt_pk_f32_fp8_e32 v[216:217], v34
	v_pk_mul_f32 v[204:205], v[204:205], v[186:187]
	v_pk_fma_f32 v[202:203], v[218:219], v[192:193], v[202:203]
	v_cvt_pk_f32_fp8_sdwa v[218:219], v34 src0_sel:WORD_1
	v_pk_fma_f32 v[204:205], v[210:211], v[190:191], v[204:205]
	v_cvt_pk_f32_fp8_e32 v[210:211], v36
	v_pk_fma_f32 v[202:203], v[220:221], v[196:197], v[202:203]
	v_cvt_pk_f32_fp8_e32 v[220:221], v35
	v_pk_fma_f32 v[204:205], v[212:213], v[194:195], v[204:205]
	v_cvt_pk_f32_fp8_sdwa v[212:213], v36 src0_sel:WORD_1
	v_cvt_pk_f32_fp8_sdwa v[222:223], v35 src0_sel:WORD_1
	v_pk_fma_f32 v[204:205], v[214:215], v[198:199], v[204:205]
	v_cvt_pk_f32_fp8_e32 v[214:215], v37
	v_pk_fma_f32 v[204:205], v[216:217], v[184:185], v[204:205]
	v_cvt_pk_f32_fp8_sdwa v[216:217], v37 src0_sel:WORD_1
	v_pk_fma_f32 v[204:205], v[218:219], v[188:189], v[204:205]
	v_cvt_pk_f32_fp8_e32 v[218:219], v38
	v_pk_mul_f32 v[210:211], v[210:211], v[186:187]
	v_pk_fma_f32 v[204:205], v[220:221], v[192:193], v[204:205]
	v_cvt_pk_f32_fp8_sdwa v[220:221], v38 src0_sel:WORD_1
	v_pk_fma_f32 v[210:211], v[212:213], v[190:191], v[210:211]
	v_cvt_pk_f32_fp8_e32 v[212:213], v40
	v_pk_fma_f32 v[204:205], v[222:223], v[196:197], v[204:205]
	v_cvt_pk_f32_fp8_e32 v[222:223], v39
	v_pk_fma_f32 v[210:211], v[214:215], v[194:195], v[210:211]
	v_cvt_pk_f32_fp8_sdwa v[214:215], v40 src0_sel:WORD_1
	v_cvt_pk_f32_fp8_sdwa v[224:225], v39 src0_sel:WORD_1
	v_pk_fma_f32 v[210:211], v[216:217], v[198:199], v[210:211]
	v_cvt_pk_f32_fp8_e32 v[216:217], v41
	v_pk_fma_f32 v[210:211], v[218:219], v[184:185], v[210:211]
	v_cvt_pk_f32_fp8_sdwa v[218:219], v41 src0_sel:WORD_1
	v_pk_fma_f32 v[210:211], v[220:221], v[188:189], v[210:211]
	v_cvt_pk_f32_fp8_e32 v[220:221], v42
	v_pk_mul_f32 v[212:213], v[212:213], v[186:187]
	v_pk_fma_f32 v[210:211], v[222:223], v[192:193], v[210:211]
	v_cvt_pk_f32_fp8_sdwa v[222:223], v42 src0_sel:WORD_1
	v_pk_fma_f32 v[212:213], v[214:215], v[190:191], v[212:213]
	v_cvt_pk_f32_fp8_e32 v[214:215], v44
	v_pk_fma_f32 v[210:211], v[224:225], v[196:197], v[210:211]
	v_cvt_pk_f32_fp8_e32 v[224:225], v43
	v_pk_fma_f32 v[212:213], v[216:217], v[194:195], v[212:213]
	v_cvt_pk_f32_fp8_sdwa v[216:217], v44 src0_sel:WORD_1
	v_cvt_pk_f32_fp8_sdwa v[226:227], v43 src0_sel:WORD_1
	v_pk_fma_f32 v[212:213], v[218:219], v[198:199], v[212:213]
	v_cvt_pk_f32_fp8_e32 v[218:219], v45
	v_pk_fma_f32 v[212:213], v[220:221], v[184:185], v[212:213]
	v_cvt_pk_f32_fp8_sdwa v[220:221], v45 src0_sel:WORD_1
	v_pk_fma_f32 v[212:213], v[222:223], v[188:189], v[212:213]
	v_cvt_pk_f32_fp8_e32 v[222:223], v46
	v_pk_mul_f32 v[214:215], v[214:215], v[186:187]
	v_pk_fma_f32 v[212:213], v[224:225], v[192:193], v[212:213]
	v_cvt_pk_f32_fp8_sdwa v[224:225], v46 src0_sel:WORD_1
	v_pk_fma_f32 v[214:215], v[216:217], v[190:191], v[214:215]
	v_cvt_pk_f32_fp8_e32 v[216:217], v48
	v_pk_fma_f32 v[212:213], v[226:227], v[196:197], v[212:213]
	v_cvt_pk_f32_fp8_e32 v[226:227], v47
	v_pk_fma_f32 v[214:215], v[218:219], v[194:195], v[214:215]
	v_cvt_pk_f32_fp8_sdwa v[218:219], v48 src0_sel:WORD_1
	v_cvt_pk_f32_fp8_sdwa v[228:229], v47 src0_sel:WORD_1
	v_pk_fma_f32 v[214:215], v[220:221], v[198:199], v[214:215]
	v_cvt_pk_f32_fp8_e32 v[220:221], v49
	v_pk_fma_f32 v[214:215], v[222:223], v[184:185], v[214:215]
	v_cvt_pk_f32_fp8_sdwa v[222:223], v49 src0_sel:WORD_1
	v_pk_fma_f32 v[214:215], v[224:225], v[188:189], v[214:215]
	v_cvt_pk_f32_fp8_e32 v[224:225], v50
	v_pk_mul_f32 v[216:217], v[216:217], v[186:187]
	v_pk_fma_f32 v[214:215], v[226:227], v[192:193], v[214:215]
	v_cvt_pk_f32_fp8_sdwa v[226:227], v50 src0_sel:WORD_1
	v_pk_fma_f32 v[216:217], v[218:219], v[190:191], v[216:217]
	v_cvt_pk_f32_fp8_e32 v[218:219], v52
	v_pk_fma_f32 v[214:215], v[228:229], v[196:197], v[214:215]
	v_cvt_pk_f32_fp8_e32 v[228:229], v51
	v_pk_fma_f32 v[216:217], v[220:221], v[194:195], v[216:217]
	v_cvt_pk_f32_fp8_sdwa v[220:221], v52 src0_sel:WORD_1
	v_cvt_pk_f32_fp8_sdwa v[230:231], v51 src0_sel:WORD_1
	v_pk_fma_f32 v[216:217], v[222:223], v[198:199], v[216:217]
	v_cvt_pk_f32_fp8_e32 v[222:223], v53
	v_pk_fma_f32 v[216:217], v[224:225], v[184:185], v[216:217]
	v_cvt_pk_f32_fp8_sdwa v[224:225], v53 src0_sel:WORD_1
	v_pk_fma_f32 v[216:217], v[226:227], v[188:189], v[216:217]
	v_cvt_pk_f32_fp8_e32 v[226:227], v54
	v_pk_mul_f32 v[218:219], v[218:219], v[186:187]
	v_pk_fma_f32 v[216:217], v[228:229], v[192:193], v[216:217]
	v_cvt_pk_f32_fp8_sdwa v[228:229], v54 src0_sel:WORD_1
	v_pk_fma_f32 v[218:219], v[220:221], v[190:191], v[218:219]
	v_cvt_pk_f32_fp8_e32 v[220:221], v56
	v_pk_fma_f32 v[216:217], v[230:231], v[196:197], v[216:217]
	v_cvt_pk_f32_fp8_e32 v[230:231], v55
	v_pk_fma_f32 v[218:219], v[222:223], v[194:195], v[218:219]
	v_cvt_pk_f32_fp8_sdwa v[222:223], v56 src0_sel:WORD_1
	v_cvt_pk_f32_fp8_sdwa v[232:233], v55 src0_sel:WORD_1
	v_pk_fma_f32 v[218:219], v[224:225], v[198:199], v[218:219]
	v_cvt_pk_f32_fp8_e32 v[224:225], v57
	v_pk_fma_f32 v[218:219], v[226:227], v[184:185], v[218:219]
	v_cvt_pk_f32_fp8_sdwa v[226:227], v57 src0_sel:WORD_1
	v_pk_fma_f32 v[218:219], v[228:229], v[188:189], v[218:219]
	v_cvt_pk_f32_fp8_e32 v[228:229], v58
	v_pk_mul_f32 v[220:221], v[220:221], v[186:187]
	v_pk_fma_f32 v[218:219], v[230:231], v[192:193], v[218:219]
	v_cvt_pk_f32_fp8_sdwa v[230:231], v58 src0_sel:WORD_1
	v_pk_fma_f32 v[220:221], v[222:223], v[190:191], v[220:221]
	v_cvt_pk_f32_fp8_e32 v[222:223], v60
	v_pk_fma_f32 v[218:219], v[232:233], v[196:197], v[218:219]
	v_cvt_pk_f32_fp8_e32 v[232:233], v59
	v_pk_fma_f32 v[220:221], v[224:225], v[194:195], v[220:221]
	v_cvt_pk_f32_fp8_sdwa v[224:225], v60 src0_sel:WORD_1
	v_cvt_pk_f32_fp8_sdwa v[234:235], v59 src0_sel:WORD_1
	v_pk_fma_f32 v[220:221], v[226:227], v[198:199], v[220:221]
	v_cvt_pk_f32_fp8_e32 v[226:227], v61
	v_pk_fma_f32 v[220:221], v[228:229], v[184:185], v[220:221]
	v_cvt_pk_f32_fp8_sdwa v[228:229], v61 src0_sel:WORD_1
	v_pk_fma_f32 v[220:221], v[230:231], v[188:189], v[220:221]
	v_cvt_pk_f32_fp8_e32 v[230:231], v62
	v_pk_mul_f32 v[222:223], v[222:223], v[186:187]
	v_pk_fma_f32 v[220:221], v[232:233], v[192:193], v[220:221]
	v_cvt_pk_f32_fp8_sdwa v[232:233], v62 src0_sel:WORD_1
	v_pk_fma_f32 v[222:223], v[224:225], v[190:191], v[222:223]
	v_cvt_pk_f32_fp8_e32 v[224:225], v76
	v_pk_fma_f32 v[220:221], v[234:235], v[196:197], v[220:221]
	v_cvt_pk_f32_fp8_e32 v[234:235], v63
	v_pk_fma_f32 v[222:223], v[226:227], v[194:195], v[222:223]
	v_cvt_pk_f32_fp8_sdwa v[226:227], v76 src0_sel:WORD_1
	v_cvt_pk_f32_fp8_sdwa v[236:237], v63 src0_sel:WORD_1
	v_pk_fma_f32 v[222:223], v[228:229], v[198:199], v[222:223]
	v_cvt_pk_f32_fp8_e32 v[228:229], v77
	v_pk_fma_f32 v[222:223], v[230:231], v[184:185], v[222:223]
	v_cvt_pk_f32_fp8_sdwa v[230:231], v77 src0_sel:WORD_1
	v_pk_fma_f32 v[222:223], v[232:233], v[188:189], v[222:223]
	v_cvt_pk_f32_fp8_e32 v[232:233], v78
	v_pk_mul_f32 v[224:225], v[224:225], v[186:187]
	v_pk_fma_f32 v[222:223], v[234:235], v[192:193], v[222:223]
	v_cvt_pk_f32_fp8_sdwa v[234:235], v78 src0_sel:WORD_1
	v_pk_fma_f32 v[224:225], v[226:227], v[190:191], v[224:225]
	v_cvt_pk_f32_fp8_e32 v[226:227], v84
	v_pk_fma_f32 v[222:223], v[236:237], v[196:197], v[222:223]
	v_cvt_pk_f32_fp8_e32 v[236:237], v79
	v_pk_fma_f32 v[224:225], v[228:229], v[194:195], v[224:225]
	v_cvt_pk_f32_fp8_sdwa v[228:229], v84 src0_sel:WORD_1
	v_cvt_pk_f32_fp8_sdwa v[238:239], v79 src0_sel:WORD_1
	v_pk_fma_f32 v[224:225], v[230:231], v[198:199], v[224:225]
	v_cvt_pk_f32_fp8_e32 v[230:231], v85
	v_pk_fma_f32 v[224:225], v[232:233], v[184:185], v[224:225]
	v_cvt_pk_f32_fp8_sdwa v[232:233], v85 src0_sel:WORD_1
	v_pk_fma_f32 v[224:225], v[234:235], v[188:189], v[224:225]
	v_cvt_pk_f32_fp8_e32 v[234:235], v86
	v_pk_mul_f32 v[226:227], v[226:227], v[186:187]
	v_pk_fma_f32 v[224:225], v[236:237], v[192:193], v[224:225]
	v_cvt_pk_f32_fp8_sdwa v[236:237], v86 src0_sel:WORD_1
	v_pk_fma_f32 v[226:227], v[228:229], v[190:191], v[226:227]
	v_cvt_pk_f32_fp8_e32 v[228:229], v88
	v_pk_fma_f32 v[224:225], v[238:239], v[196:197], v[224:225]
	v_cvt_pk_f32_fp8_e32 v[238:239], v87
	v_pk_fma_f32 v[226:227], v[230:231], v[194:195], v[226:227]
	v_cvt_pk_f32_fp8_sdwa v[230:231], v88 src0_sel:WORD_1
	v_cvt_pk_f32_fp8_sdwa v[240:241], v87 src0_sel:WORD_1
	v_pk_fma_f32 v[226:227], v[232:233], v[198:199], v[226:227]
	v_cvt_pk_f32_fp8_e32 v[232:233], v89
	v_pk_fma_f32 v[226:227], v[234:235], v[184:185], v[226:227]
	v_cvt_pk_f32_fp8_sdwa v[234:235], v89 src0_sel:WORD_1
	v_pk_fma_f32 v[226:227], v[236:237], v[188:189], v[226:227]
	v_cvt_pk_f32_fp8_e32 v[236:237], v90
	v_pk_mul_f32 v[228:229], v[228:229], v[186:187]
	v_pk_fma_f32 v[226:227], v[238:239], v[192:193], v[226:227]
	v_cvt_pk_f32_fp8_sdwa v[238:239], v90 src0_sel:WORD_1
	v_pk_fma_f32 v[228:229], v[230:231], v[190:191], v[228:229]
	v_cvt_pk_f32_fp8_e32 v[230:231], v92
	v_pk_fma_f32 v[226:227], v[240:241], v[196:197], v[226:227]
	v_cvt_pk_f32_fp8_e32 v[240:241], v91
	v_pk_fma_f32 v[228:229], v[232:233], v[194:195], v[228:229]
	v_cvt_pk_f32_fp8_sdwa v[232:233], v92 src0_sel:WORD_1
	v_cvt_pk_f32_fp8_sdwa v[242:243], v91 src0_sel:WORD_1
	v_pk_fma_f32 v[228:229], v[234:235], v[198:199], v[228:229]
	v_cvt_pk_f32_fp8_e32 v[234:235], v93
	v_pk_fma_f32 v[228:229], v[236:237], v[184:185], v[228:229]
	v_cvt_pk_f32_fp8_sdwa v[236:237], v93 src0_sel:WORD_1
	v_pk_fma_f32 v[228:229], v[238:239], v[188:189], v[228:229]
	v_cvt_pk_f32_fp8_e32 v[238:239], v94
	v_pk_mul_f32 v[230:231], v[230:231], v[186:187]
	v_pk_fma_f32 v[228:229], v[240:241], v[192:193], v[228:229]
	v_cvt_pk_f32_fp8_sdwa v[240:241], v94 src0_sel:WORD_1
	v_pk_fma_f32 v[230:231], v[232:233], v[190:191], v[230:231]
	v_cvt_pk_f32_fp8_e32 v[232:233], v96
	v_pk_fma_f32 v[228:229], v[242:243], v[196:197], v[228:229]
	v_cvt_pk_f32_fp8_e32 v[242:243], v95
	v_pk_fma_f32 v[230:231], v[234:235], v[194:195], v[230:231]
	v_cvt_pk_f32_fp8_sdwa v[234:235], v96 src0_sel:WORD_1
	v_cvt_pk_f32_fp8_sdwa v[244:245], v95 src0_sel:WORD_1
	v_pk_fma_f32 v[230:231], v[236:237], v[198:199], v[230:231]
	v_cvt_pk_f32_fp8_e32 v[236:237], v97
	v_pk_fma_f32 v[230:231], v[238:239], v[184:185], v[230:231]
	v_cvt_pk_f32_fp8_sdwa v[238:239], v97 src0_sel:WORD_1
	v_pk_fma_f32 v[230:231], v[240:241], v[188:189], v[230:231]
	v_cvt_pk_f32_fp8_e32 v[240:241], v98
	v_pk_mul_f32 v[232:233], v[232:233], v[186:187]
	v_pk_fma_f32 v[230:231], v[242:243], v[192:193], v[230:231]
	v_cvt_pk_f32_fp8_sdwa v[242:243], v98 src0_sel:WORD_1
	v_pk_fma_f32 v[232:233], v[234:235], v[190:191], v[232:233]
	v_cvt_pk_f32_fp8_e32 v[234:235], v104
	v_pk_fma_f32 v[230:231], v[244:245], v[196:197], v[230:231]
	v_cvt_pk_f32_fp8_e32 v[244:245], v99
	v_pk_fma_f32 v[232:233], v[236:237], v[194:195], v[232:233]
	v_cvt_pk_f32_fp8_sdwa v[236:237], v104 src0_sel:WORD_1
	v_cvt_pk_f32_fp8_sdwa v[246:247], v99 src0_sel:WORD_1
	v_pk_fma_f32 v[232:233], v[238:239], v[198:199], v[232:233]
	v_cvt_pk_f32_fp8_e32 v[238:239], v105
	v_pk_fma_f32 v[232:233], v[240:241], v[184:185], v[232:233]
	v_cvt_pk_f32_fp8_sdwa v[240:241], v105 src0_sel:WORD_1
	v_pk_fma_f32 v[232:233], v[242:243], v[188:189], v[232:233]
	v_cvt_pk_f32_fp8_e32 v[242:243], v106
	v_pk_mul_f32 v[186:187], v[234:235], v[186:187]
	v_pk_fma_f32 v[232:233], v[244:245], v[192:193], v[232:233]
	v_cvt_pk_f32_fp8_sdwa v[244:245], v106 src0_sel:WORD_1
	v_pk_fma_f32 v[186:187], v[236:237], v[190:191], v[186:187]
	v_pk_fma_f32 v[232:233], v[246:247], v[196:197], v[232:233]
	v_cvt_pk_f32_fp8_e32 v[246:247], v107
	v_pk_fma_f32 v[186:187], v[238:239], v[194:195], v[186:187]
	v_cvt_pk_f32_fp8_sdwa v[248:249], v107 src0_sel:WORD_1
	v_pk_fma_f32 v[186:187], v[240:241], v[198:199], v[186:187]
	v_mov_b32_e32 v194, v220
	v_pk_fma_f32 v[184:185], v[242:243], v[184:185], v[186:187]
	v_mov_b32_e32 v186, v200
	v_pk_fma_f32 v[184:185], v[244:245], v[188:189], v[184:185]
	v_mov_b32_e32 v187, v202
	v_pk_fma_f32 v[184:185], v[246:247], v[192:193], v[184:185]
	v_mov_b32_e32 v202, v201
	v_pk_fma_f32 v[184:185], v[248:249], v[196:197], v[184:185]
	v_mov_b32_e32 v195, v222
	v_mov_b32_e32 v222, v221
	v_pk_add_f32 v[186:187], v[186:187], v[202:203]
	v_pk_add_f32 v[194:195], v[194:195], v[222:223]
	v_mov_b32_e32 v200, v232
	v_mov_b32_e32 v201, v184
	v_mov_b32_e32 v184, v233
	v_mov_b32_e32 v188, v204
	v_mov_b32_e32 v189, v210
	v_mov_b32_e32 v210, v205
	v_mov_b32_e32 v196, v224
	v_mov_b32_e32 v197, v226
	v_mov_b32_e32 v226, v225
	v_pk_add_f32 v[184:185], v[200:201], v[184:185]
	v_cndmask_b32_e64 v200, v186, v194, s[4:5]
	v_cndmask_b32_e64 v202, v194, v186, s[4:5]
	v_cndmask_b32_e64 v186, v187, v195, s[4:5]
	v_pk_add_f32 v[188:189], v[188:189], v[210:211]
	v_pk_add_f32 v[196:197], v[196:197], v[226:227]
	v_mov_b32_dpp v200, v200 row_half_mirror row_mask:0xf bank_mask:0xf bound_ctrl:1
	v_cndmask_b32_e64 v203, v195, v187, s[4:5]
	v_mov_b32_dpp v201, v186 row_half_mirror row_mask:0xf bank_mask:0xf bound_ctrl:1
	v_mov_b32_e32 v190, v212
	v_mov_b32_e32 v191, v214
	v_mov_b32_e32 v214, v213
	v_mov_b32_e32 v198, v228
	v_mov_b32_e32 v199, v230
	v_mov_b32_e32 v230, v229
	v_pk_add_f32 v[186:187], v[202:203], v[200:201]
	v_cndmask_b32_e64 v194, v188, v196, s[4:5]
	v_cndmask_b32_e64 v200, v196, v188, s[4:5]
	v_cndmask_b32_e64 v188, v189, v197, s[4:5]
	v_pk_add_f32 v[190:191], v[190:191], v[214:215]
	v_pk_add_f32 v[198:199], v[198:199], v[230:231]
	v_mov_b32_dpp v194, v194 row_half_mirror row_mask:0xf bank_mask:0xf bound_ctrl:1
	v_cndmask_b32_e64 v201, v197, v189, s[4:5]
	v_mov_b32_dpp v195, v188 row_half_mirror row_mask:0xf bank_mask:0xf bound_ctrl:1
	v_mov_b32_e32 v192, v216
	v_mov_b32_e32 v193, v218
	v_mov_b32_e32 v218, v217
	v_pk_add_f32 v[188:189], v[200:201], v[194:195]
	v_cndmask_b32_e64 v194, v190, v198, s[4:5]
	v_cndmask_b32_e64 v196, v198, v190, s[4:5]
	v_cndmask_b32_e64 v190, v191, v199, s[4:5]
	v_pk_add_f32 v[192:193], v[192:193], v[218:219]
	v_mov_b32_dpp v194, v194 row_half_mirror row_mask:0xf bank_mask:0xf bound_ctrl:1
	v_cndmask_b32_e64 v197, v199, v191, s[4:5]
	v_mov_b32_dpp v195, v190 row_half_mirror row_mask:0xf bank_mask:0xf bound_ctrl:1
	v_pk_add_f32 v[190:191], v[196:197], v[194:195]
	v_cndmask_b32_e64 v194, v192, v184, s[4:5]
	v_cndmask_b32_e64 v196, v184, v192, s[4:5]
	v_cndmask_b32_e64 v184, v193, v185, s[4:5]
	v_mov_b32_dpp v194, v194 row_half_mirror row_mask:0xf bank_mask:0xf bound_ctrl:1
	v_cndmask_b32_e64 v197, v185, v193, s[4:5]
	v_mov_b32_dpp v195, v184 row_half_mirror row_mask:0xf bank_mask:0xf bound_ctrl:1
	v_pk_add_f32 v[184:185], v[196:197], v[194:195]
	v_cndmask_b32_e64 v192, v186, v190, s[2:3]
	v_cndmask_b32_e64 v194, v190, v186, s[2:3]
	v_cndmask_b32_e64 v186, v187, v191, s[2:3]
	v_mov_b32_dpp v192, v192 quad_perm:[2,3,0,1] row_mask:0xf bank_mask:0xf bound_ctrl:1
	v_cndmask_b32_e64 v195, v191, v187, s[2:3]
	v_mov_b32_dpp v193, v186 quad_perm:[2,3,0,1] row_mask:0xf bank_mask:0xf bound_ctrl:1
	v_pk_add_f32 v[186:187], v[194:195], v[192:193]
	v_cndmask_b32_e64 v190, v188, v184, s[2:3]
	v_cndmask_b32_e64 v192, v184, v188, s[2:3]
	v_cndmask_b32_e64 v184, v189, v185, s[2:3]
	v_mov_b32_dpp v190, v190 quad_perm:[2,3,0,1] row_mask:0xf bank_mask:0xf bound_ctrl:1
	v_cndmask_b32_e64 v193, v185, v189, s[2:3]
	v_mov_b32_dpp v191, v184 quad_perm:[2,3,0,1] row_mask:0xf bank_mask:0xf bound_ctrl:1
	v_pk_add_f32 v[184:185], v[192:193], v[190:191]
	s_ashr_i32 s15, s14, 31
	v_cndmask_b32_e64 v188, v186, v184, s[0:1]
	v_cndmask_b32_e64 v190, v184, v186, s[0:1]
	v_cndmask_b32_e64 v184, v187, v185, s[0:1]
	v_mov_b32_dpp v188, v188 quad_perm:[1,0,3,2] row_mask:0xf bank_mask:0xf bound_ctrl:1
	v_cndmask_b32_e64 v191, v185, v187, s[0:1]
	v_mov_b32_dpp v189, v184 quad_perm:[1,0,3,2] row_mask:0xf bank_mask:0xf bound_ctrl:1
	v_pk_add_f32 v[184:185], v[190:191], v[188:189]
	s_lshl_b64 s[14:15], s[14:15], 8
	v_cvt_pk_bf16_f32 v186, v184, v185
	v_lshl_add_u64 v[184:185], v[178:179], 0, s[14:15]
	s_cmpk_gt_i32 s10, 0x7fff
	s_mov_b64 s[22:23], -1
	global_store_dword v[184:185], v186, off
	s_cbranch_scc1 .LBB0_1740
; #define PD_H(t, H) do { const char* hb_ = h2u + (size_t)(t) * 2048; H[0] = *(const u32x4*)(hb_ + h2o); H[1] = *(const u32x4*)(hb_ + (h2o + 16u)); } while (0)
; #define PD_TAB(E, W) do { _Pragma("unroll") for (int q = 0; q < 16; ++q) W[q] = *(const u32x4*)(tabu + ((unsigned)E[q >> 2][q & 3] * 128u + tabo)); } while (0)
; DI void phase_peerdown(const Params& p, int bid, int nb) {
;     ...
;     if (t2 < T_) { PD_H(t2, hA); PD_TAB(eA, wA); }
	s_andn2_b64 vcc, exec, s[20:21]
	s_cbranch_vccnz .LBB0_1748
	s_ashr_i32 s9, s8, 31
	s_lshl_b64 s[14:15], s[8:9], 11
	v_lshl_add_u64 v[24:25], v[182:183], 0, s[14:15]
	global_load_dwordx4 v[16:19], v[24:25], off offset:16
	global_load_dwordx4 v[20:23], v[24:25], off
	s_waitcnt vmcnt(2)
	v_lshl_or_b32 v24, v0, 7, v209
	v_lshl_or_b32 v28, v1, 7, v209
	v_lshl_or_b32 v32, v2, 7, v209
	v_lshl_or_b32 v36, v3, 7, v209
	v_lshl_or_b32 v40, v4, 7, v209
	v_lshl_or_b32 v44, v5, 7, v209
	v_lshl_or_b32 v48, v6, 7, v209
	v_lshl_or_b32 v52, v7, 7, v209
	v_lshl_or_b32 v56, v8, 7, v209
	v_lshl_or_b32 v60, v9, 7, v209
	v_lshl_or_b32 v76, v10, 7, v209
	v_lshl_or_b32 v84, v11, 7, v209
	v_lshl_or_b32 v88, v12, 7, v209
	v_lshl_or_b32 v92, v13, 7, v209
	v_lshl_or_b32 v96, v14, 7, v209
	v_lshl_or_b32 v104, v15, 7, v209
	global_load_dwordx4 v[24:27], v24, s[6:7]
	s_nop 0
	global_load_dwordx4 v[28:31], v28, s[6:7]
	s_nop 0
	global_load_dwordx4 v[32:35], v32, s[6:7]
	s_nop 0
	global_load_dwordx4 v[36:39], v36, s[6:7]
	s_nop 0
	global_load_dwordx4 v[40:43], v40, s[6:7]
	s_nop 0
	global_load_dwordx4 v[44:47], v44, s[6:7]
	s_nop 0
	global_load_dwordx4 v[48:51], v48, s[6:7]
	s_nop 0
	global_load_dwordx4 v[52:55], v52, s[6:7]
	s_nop 0
	global_load_dwordx4 v[56:59], v56, s[6:7]
	s_nop 0
	global_load_dwordx4 v[60:63], v60, s[6:7]
	s_nop 0
	global_load_dwordx4 v[76:79], v76, s[6:7]
	s_nop 0
	global_load_dwordx4 v[84:87], v84, s[6:7]
	s_nop 0
	global_load_dwordx4 v[88:91], v88, s[6:7]
	s_nop 0
	global_load_dwordx4 v[92:95], v92, s[6:7]
	s_nop 0
	global_load_dwordx4 v[96:99], v96, s[6:7]
	s_nop 0
	global_load_dwordx4 v[104:107], v104, s[6:7]
